# layer-0 sparse items: a workgroup's four items now cover four different 512-query blocks (block ^ 2*round), so every workgroup walks 64 key tiles instead of 56..68
# baseline (speedup 1.0000x reference)
; #define LAS __attribute__((address_space(3)))
; __device__ __forceinline__ int fresh_tid(int wv) { int l; asm volatile("v_mbcnt_lo_u32_b32 %0, -1, 0\n\tv_mbcnt_hi_u32_b32 %0, -1, %0" : "=v"(l)); return wv * 64 + l; }
;     __device__ __forceinline__ void init(const bf16_t* H0_, bf16_t* O_, const unsigned char* K8_, const unsigned char* Vt1_, const unsigned char* Vt4_, const unsigned char* Vt16_, int w, int lane) {
;         H0 = H0_; O = O_; K8 = K8_; Vt1 = Vt1_; Vt4 = Vt4_; Vt16 = Vt16_; b = w >> 10; h = (w >> 7) & 7; const int wu = w & 127; a = wu >> 4; r16 = wu & 15; myn = lane & 31; hi32 = 32 * (lane >> 5);
;         const int t = a >> 1; lo3 = max(t - 1, 0); n3 = min(t + 1, 3) - lo3 + 1;
;         lo2 = max(2 * a - 1, 0); n2 = min(2 * a + 2, 15) - lo2 + 1;
;         lo1 = max(8 * a - 1, 0); n1 = min(8 * a + 8, 63) - lo1 + 1;
;         slope2 = __builtin_amdgcn_exp2f(-(float)(h + 1)) * LOG2E;
;     }
; __global__ void __launch_bounds__(NTHR, 2) fwd(Params p) {
;     ...
;                 for (int it = vcu; it < 1024; it += G) {
;                     const int tid2 = fresh_tid(wv), wid = __builtin_amdgcn_readfirstlane(tid2 >> 6), lane = tid2 & 63;
;                     const int w = it * 8 + wid; LAS unsigned char* wl = lds + wid * da::SP_WAVE_LDS;
;                     if constexpr (F8_SPARSE) { const unsigned char* ra8 = (const unsigned char*)RA; PolB8 pol; pol.init(Hx, Oat, ra8, ra8 + 32 * MiB, ra8 + 64 * MiB, ra8 + 96 * MiB, w, lane); d8::sparse8_wave(pol, wl, lane); }
.LBB0_545:
	v_mbcnt_lo_u32_b32 v32, -1, 0
	v_mbcnt_hi_u32_b32 v32, -1, v32
	s_lshl_b32 s0, s56, 3
	v_add_u32_e32 v0, s5, v32
	s_nop 0
	v_readfirstlane_b32 s38, v0
	s_ashr_i32 s8, s38, 6
	s_add_i32 s33, s8, s0
	s_lshr_b32 s1, s56, 8
	s_lshl_b32 s1, s1, 5
	s_xor_b32 s33, s33, s1
	s_lshr_b32 s0, s33, 4
	s_bfe_u32 s1, s0, 0x20001
	s_bfe_u32 s39, s33, 0x30004
	s_max_u32 s0, s1, 1
	s_min_u32 s1, s1, 2
	s_sub_i32 s9, s1, s0
	s_lshl_b32 s41, s39, 3
	s_and_b32 s15, s33, 15
	s_add_i32 s59, s9, 3
	v_sub_u32_e64 v0, s41, 1 clamp
	s_cmp_eq_u32 s59, 0
	v_readfirstlane_b32 s23, v0
	s_cbranch_scc1 .LBB0_547
	s_lshl_b32 s0, s0, 6
	s_lshl_b32 s1, s15, 8
	s_sub_i32 s24, s0, 64
	s_add_i32 s40, s24, s1
	s_mov_b64 s[0:1], 0
	s_branch .LBB0_548

; #define SBAR() __builtin_amdgcn_sched_barrier(0)
; #define SBAR() __builtin_amdgcn_sched_barrier(0)
; #define SP8_DMA_V(T) do { const unsigned char* vb_ = SP8_UNI((T).v); \
;         _Pragma("unroll") for (int i = 0; i < 8; ++i) { const unsigned char* src = vb_ + (unsigned long long)(16 * i) * SEQ + voff; \
;         __builtin_amdgcn_global_load_lds((const unsigned*)src, (LAS unsigned*)(wll + 8192 + i * 1024), 16, 0, 0); } } while (0)
; template <class P>
; __device__ __forceinline__ void sparse8_wave(P& pol, LAS unsigned char* wll, int lane) {
;     ...
;     const int a0k = 32 * ((lane >> 5) & 1) + ((lane >> 3) & 3), che = (((lane & 7) ^ (lane >> 4)) & 7) << 4, cho = che ^ 64;
;     const int vcol0 = lane >> 2; const unsigned voff = (unsigned)vcol0 * SEQ + ((((lane & 3) ^ (vcol0 >> 2)) & 3) << 4);
;     const int nt = pol.ntiles();
;     typename P::TI ti, tn;
;     ...
;     pol.tile(0, ti);
;     SP8_DMA_K(ti); SP8_DMA_V(ti);
;     pol.pre_issue(); SBAR();
;     i32x8 qf[2];
;     { const bf16_t* Qw = pol.qptr(r32); u32x4 qv[2][4];
; #pragma unroll
;       for (int sK = 0; sK < 2; ++sK)
; #pragma unroll
;           for (int c = 0; c < 4; ++c) qv[sK][c] = *(const u32x4*)(Qw + 64 * sK + 32 * hi + 8 * c);
.LBB0_553:
	v_and_b32_e32 v163, 63, v32
	v_and_b32_e32 v165, 32, v32
	v_lshrrev_b32_e32 v0, 3, v32
	s_mul_i32 s0, s8, 0x4900
	v_and_or_b32 v166, v0, 3, v165
	v_lshlrev_b32_e32 v0, 4, v163
	s_add_i32 s61, s0, 0
	s_ashr_i32 s0, s33, 10
	s_bfe_u32 s38, s33, 0x30007
	s_min_u32 s1, s41, 55
	v_bitop3_b32 v34, v0, v32, 63 bitop3:0x78
	v_bitop3_b32 v167, v0, s89, v163 bitop3:0x48
	v_lshlrev_b32_e32 v0, 10, v32
	s_mov_b32 s33, 0xf030
	v_bitop3_b32 v232, v34, s33, v0 bitop3:0xc8
	s_sub_i32 s1, s1, s42
	s_mul_i32 s33, s29, s24
	s_add_i32 s62, s1, s60
	s_ashr_i32 s1, s0, 31
	s_add_i32 s36, s33, s25
	s_add_i32 s62, s62, 10
	s_lshl_b64 s[42:43], s[0:1], 22
	s_lshl_b64 s[48:49], s[36:37], 10
	s_add_u32 s1, s52, s42
	s_addc_u32 s33, s53, s43
	s_add_u32 s41, s1, s48
	s_addc_u32 s43, s33, s49
	s_lshl_b32 s36, s38, 7
	s_add_u32 s42, s41, s36
	s_addc_u32 s43, s43, 0
	s_lshl_b32 s41, s0, 3
	s_or_b32 s48, s38, s41
	s_ashr_i32 s49, s48, 31
	s_lshl_b64 s[72:73], s[48:49], 19
	v_mul_lo_u32 v0, s29, v166
	s_lshl_b32 s41, s29, 12
	v_lshlrev_b32_e32 v0, 10, v0
	s_add_u32 s48, s42, s41
	v_or_b32_e32 v1, v0, v167
	s_mov_b32 m0, s61
	s_addc_u32 s49, s43, 0
	s_add_i32 s63, s61, 0x400
	global_load_lds_dwordx4 v1, s[42:43]
	v_bitop3_b32 v0, v0, v167, 64 bitop3:0xf6
	s_mov_b32 m0, s63
	s_lshl_b32 s41, s29, 13
	global_load_lds_dwordx4 v0, s[48:49]
	s_add_u32 s48, s42, s41
	s_addc_u32 s49, s43, 0
	s_add_i32 s64, s61, 0x800
	s_mov_b32 m0, s64
	s_mul_i32 s41, s29, 0x3000
	global_load_lds_dwordx4 v1, s[48:49]
	s_add_u32 s48, s42, s41
	s_addc_u32 s49, s43, 0
	s_add_i32 s65, s61, 0xc00
	s_mov_b32 m0, s65
	s_lshl_b32 s41, s29, 14
	global_load_lds_dwordx4 v0, s[48:49]
	s_add_u32 s48, s42, s41
	s_addc_u32 s49, s43, 0
	s_add_i32 s66, s61, 0x1000
	s_mov_b32 m0, s66
	s_mul_i32 s41, s29, 0x5000
	global_load_lds_dwordx4 v1, s[48:49]
	s_add_u32 s48, s42, s41
	s_addc_u32 s49, s43, 0
	s_add_i32 s67, s61, 0x1400
	s_mov_b32 m0, s67
	s_mul_i32 s41, s29, 0x6000
	global_load_lds_dwordx4 v0, s[48:49]
	s_add_u32 s48, s42, s41
	s_addc_u32 s49, s43, 0
	s_add_i32 s86, s61, 0x1800
	s_mul_i32 s41, s29, 0x7000
	s_add_u32 s42, s42, s41
	s_addc_u32 s43, s43, 0
	s_add_i32 s87, s61, 0x1c00
	s_add_u32 s6, s6, s72
	s_addc_u32 s7, s7, s73
	s_mov_b32 m0, s86
	s_add_u32 s6, s6, s40
	global_load_lds_dwordx4 v1, s[48:49]
	s_mov_b32 m0, s87
	s_addc_u32 s7, s7, 0
	s_add_i32 s92, s61, 0x2000
	global_load_lds_dwordx4 v0, s[42:43]
	s_mov_b32 m0, s92
	v_lshl_add_u64 v[0:1], s[6:7], 0, v[232:233]
	global_load_lds_dwordx4 v232, s[6:7]
	s_mov_b64 s[6:7], 0x10000
	s_add_i32 s93, s61, 0x2400
	v_lshl_add_u64 v[2:3], v[0:1], 0, s[6:7]
	s_mov_b32 m0, s93
	s_add_i32 s94, s61, 0x2800
	global_load_lds_dwordx4 v[2:3], off
	v_lshl_add_u64 v[2:3], v[0:1], 0, s[26:27]
	s_mov_b32 m0, s94
	s_mov_b64 s[6:7], 0x30000
	s_add_i32 s95, s61, 0x2c00
	global_load_lds_dwordx4 v[2:3], off
	v_lshl_add_u64 v[2:3], v[0:1], 0, s[6:7]
	s_mov_b32 m0, s95
	s_mov_b64 s[6:7], 0x40000
	s_add_i32 s96, s61, 0x3000
	global_load_lds_dwordx4 v[2:3], off
	v_lshl_add_u64 v[2:3], v[0:1], 0, s[6:7]
	s_mov_b32 m0, s96
	s_mov_b64 s[6:7], 0x50000
	s_add_i32 s97, s61, 0x3400
	global_load_lds_dwordx4 v[2:3], off
	v_lshl_add_u64 v[2:3], v[0:1], 0, s[6:7]
	s_mov_b32 m0, s97
	s_mov_b64 s[6:7], 0x60000
	s_add_i32 s48, s61, 0x3800
	global_load_lds_dwordx4 v[2:3], off
	v_lshl_add_u64 v[2:3], v[0:1], 0, s[6:7]
	s_mov_b32 m0, s48
	s_mov_b64 s[6:7], 0x70000
	s_add_i32 s49, s61, 0x3c00
	global_load_lds_dwordx4 v[2:3], off
	v_lshl_add_u64 v[0:1], v[0:1], 0, s[6:7]
	s_mov_b32 m0, s49
	v_and_b32_e32 v160, 31, v32
	global_load_lds_dwordx4 v[0:1], off
	v_bfe_u32 v161, v32, 5, 1
	s_lshl_b32 s58, s0, 12
	v_lshl_or_b32 v33, v160, 4, s15
	s_lshl_b32 s57, s39, 9
	v_or_b32_e32 v0, s58, v33
	v_or_b32_e32 v2, s57, v0
	v_mov_b64_e32 v[0:1], s[68:69]
	s_movk_i32 s0, 0x2400
	v_mad_i64_i32 v[0:1], s[6:7], v2, s0, v[0:1]
	s_lshl_b32 s6, s38, 8
	s_mov_b32 s7, s37
	v_lshl_add_u64 v[0:1], v[0:1], 0, s[6:7]
	v_lshlrev_b32_e32 v2, 1, v165
	v_mov_b32_e32 v3, v233
	v_lshl_add_u64 v[12:13], v[0:1], 0, v[2:3]
	global_load_dwordx4 v[16:19], v[12:13], off offset:3120
	global_load_dwordx4 v[20:23], v[12:13], off offset:3104
	global_load_dwordx4 v[24:27], v[12:13], off offset:3088
	global_load_dwordx4 v[28:31], v[12:13], off offset:3072
	global_load_dwordx4 v[0:3], v[12:13], off offset:3248
	global_load_dwordx4 v[4:7], v[12:13], off offset:3232
	global_load_dwordx4 v[8:11], v[12:13], off offset:3216
	s_nop 0
	global_load_dwordx4 v[12:15], v[12:13], off offset:3200
	s_cmp_lt_i32 s62, 1
	s_cbranch_scc1 .LBB0_579
; __device__ __forceinline__ float bflo(unsigned w) { return __uint_as_float(w << 16); }
; __device__ __forceinline__ float bfhi(unsigned w) { return __uint_as_float(w & 0xffff0000u); }
; #define SBAR() __builtin_amdgcn_sched_barrier(0)
; #define SBAR() __builtin_amdgcn_sched_barrier(0)
; template <class P>
; __device__ __forceinline__ void sparse8_wave(P& pol, LAS unsigned char* wll, int lane) {
;     ...
;       SBAR();
; #pragma unroll
;       for (int sK = 0; sK < 2; ++sK) { unsigned w[8];
; #pragma unroll
;           for (int c = 0; c < 4; ++c) { const u32x4 v = qv[sK][c];
;               w[2 * c] = pk4_fp8(bflo(v.x) * QCS, bfhi(v.x) * QCS, bflo(v.y) * QCS, bfhi(v.y) * QCS); w[2 * c + 1] = pk4_fp8(bflo(v.z) * QCS, bfhi(v.z) * QCS, bflo(v.w) * QCS, bfhi(v.w) * QCS); }
;           qf[sK] = (i32x8){(int)w[0], (int)w[1], (int)w[2], (int)w[3], (int)w[4], (int)w[5], (int)w[6], (int)w[7]}; } }
	v_mov_b32_e32 v35, 0x70
	v_bitop3_b32 v168, v34, 64, v35 bitop3:0x6c
	s_waitcnt vmcnt(0)
	v_lshlrev_b32_e32 v34, 16, v28
	v_and_b32_e32 v28, 0xffff0000, v28
	v_mul_f32_e32 v128, 0x3e0293ee, v34
	v_mul_f32_e32 v28, 0x3e0293ee, v28
	v_cvt_pk_fp8_f32 v128, v128, v28
	v_lshlrev_b32_e32 v34, 16, v29
	v_and_b32_e32 v29, 0xffff0000, v29
	v_mul_f32_e32 v28, 0x3e0293ee, v34
	v_mul_f32_e32 v29, 0x3e0293ee, v29
	v_cvt_pk_fp8_f32 v128, v28, v29 op_sel:[0,0,1]
	v_lshlrev_b32_e32 v28, 16, v30
	v_mul_f32_e32 v129, 0x3e0293ee, v28
	v_and_b32_e32 v28, 0xffff0000, v30
	v_mul_f32_e32 v28, 0x3e0293ee, v28
	v_cvt_pk_fp8_f32 v129, v129, v28
	v_lshlrev_b32_e32 v29, 16, v31
	v_mul_f32_e32 v28, 0x3e0293ee, v29
	v_and_b32_e32 v29, 0xffff0000, v31
	v_mul_f32_e32 v29, 0x3e0293ee, v29
	v_cvt_pk_fp8_f32 v129, v28, v29 op_sel:[0,0,1]
	v_lshlrev_b32_e32 v28, 16, v24
	v_and_b32_e32 v24, 0xffff0000, v24
	v_mul_f32_e32 v130, 0x3e0293ee, v28
	v_mul_f32_e32 v24, 0x3e0293ee, v24
	v_cvt_pk_fp8_f32 v130, v130, v24
	v_lshlrev_b32_e32 v28, 16, v25
	v_and_b32_e32 v25, 0xffff0000, v25
	v_mul_f32_e32 v24, 0x3e0293ee, v28
	v_mul_f32_e32 v25, 0x3e0293ee, v25
	v_cvt_pk_fp8_f32 v130, v24, v25 op_sel:[0,0,1]
	v_lshlrev_b32_e32 v24, 16, v26
	v_mul_f32_e32 v131, 0x3e0293ee, v24
	v_and_b32_e32 v24, 0xffff0000, v26
	v_mul_f32_e32 v24, 0x3e0293ee, v24
	v_cvt_pk_fp8_f32 v131, v131, v24
	v_lshlrev_b32_e32 v25, 16, v27
	v_mul_f32_e32 v24, 0x3e0293ee, v25
	v_and_b32_e32 v25, 0xffff0000, v27
	v_mul_f32_e32 v25, 0x3e0293ee, v25
	v_cvt_pk_fp8_f32 v131, v24, v25 op_sel:[0,0,1]
	v_lshlrev_b32_e32 v24, 16, v20
	v_and_b32_e32 v20, 0xffff0000, v20
	v_mul_f32_e32 v132, 0x3e0293ee, v24
	v_mul_f32_e32 v20, 0x3e0293ee, v20
	v_cvt_pk_fp8_f32 v132, v132, v20
	v_lshlrev_b32_e32 v24, 16, v21
	v_and_b32_e32 v21, 0xffff0000, v21
	v_mul_f32_e32 v20, 0x3e0293ee, v24
	v_mul_f32_e32 v21, 0x3e0293ee, v21
	v_cvt_pk_fp8_f32 v132, v20, v21 op_sel:[0,0,1]
	v_lshlrev_b32_e32 v20, 16, v22
	v_mul_f32_e32 v133, 0x3e0293ee, v20
	v_and_b32_e32 v20, 0xffff0000, v22
	v_mul_f32_e32 v20, 0x3e0293ee, v20
	v_cvt_pk_fp8_f32 v133, v133, v20
	v_lshlrev_b32_e32 v21, 16, v23
	v_mul_f32_e32 v20, 0x3e0293ee, v21
	v_and_b32_e32 v21, 0xffff0000, v23
	v_mul_f32_e32 v21, 0x3e0293ee, v21
	v_cvt_pk_fp8_f32 v133, v20, v21 op_sel:[0,0,1]
	v_lshlrev_b32_e32 v20, 16, v16
	v_and_b32_e32 v16, 0xffff0000, v16
	v_mul_f32_e32 v134, 0x3e0293ee, v20
	v_mul_f32_e32 v16, 0x3e0293ee, v16
	v_cvt_pk_fp8_f32 v134, v134, v16
	v_lshlrev_b32_e32 v20, 16, v17
	v_and_b32_e32 v17, 0xffff0000, v17
	v_mul_f32_e32 v16, 0x3e0293ee, v20
	v_mul_f32_e32 v17, 0x3e0293ee, v17
	v_cvt_pk_fp8_f32 v134, v16, v17 op_sel:[0,0,1]
	v_lshlrev_b32_e32 v16, 16, v18
	v_mul_f32_e32 v135, 0x3e0293ee, v16
	v_and_b32_e32 v16, 0xffff0000, v18
	v_mul_f32_e32 v16, 0x3e0293ee, v16
	v_cvt_pk_fp8_f32 v135, v135, v16
	v_lshlrev_b32_e32 v17, 16, v19
	v_mul_f32_e32 v16, 0x3e0293ee, v17
	v_and_b32_e32 v17, 0xffff0000, v19
	v_mul_f32_e32 v17, 0x3e0293ee, v17
	v_cvt_pk_fp8_f32 v135, v16, v17 op_sel:[0,0,1]
	v_lshlrev_b32_e32 v16, 16, v12
	v_and_b32_e32 v12, 0xffff0000, v12
	v_mul_f32_e32 v136, 0x3e0293ee, v16
	v_mul_f32_e32 v12, 0x3e0293ee, v12
	v_cvt_pk_fp8_f32 v136, v136, v12
	v_lshlrev_b32_e32 v16, 16, v13
	v_and_b32_e32 v13, 0xffff0000, v13
	v_mul_f32_e32 v12, 0x3e0293ee, v16
	v_mul_f32_e32 v13, 0x3e0293ee, v13
	v_cvt_pk_fp8_f32 v136, v12, v13 op_sel:[0,0,1]
	v_lshlrev_b32_e32 v12, 16, v14
	v_mul_f32_e32 v137, 0x3e0293ee, v12
	v_and_b32_e32 v12, 0xffff0000, v14
	v_mul_f32_e32 v12, 0x3e0293ee, v12
	v_cvt_pk_fp8_f32 v137, v137, v12
	v_lshlrev_b32_e32 v13, 16, v15
	v_mul_f32_e32 v12, 0x3e0293ee, v13
	v_and_b32_e32 v13, 0xffff0000, v15
	v_mul_f32_e32 v13, 0x3e0293ee, v13
	v_cvt_pk_fp8_f32 v137, v12, v13 op_sel:[0,0,1]
	v_lshlrev_b32_e32 v12, 16, v8
	v_and_b32_e32 v8, 0xffff0000, v8
	v_mul_f32_e32 v138, 0x3e0293ee, v12
	v_mul_f32_e32 v8, 0x3e0293ee, v8
	v_cvt_pk_fp8_f32 v138, v138, v8
	v_lshlrev_b32_e32 v12, 16, v9
	v_and_b32_e32 v9, 0xffff0000, v9
	v_mul_f32_e32 v8, 0x3e0293ee, v12
	v_mul_f32_e32 v9, 0x3e0293ee, v9
	v_cvt_pk_fp8_f32 v138, v8, v9 op_sel:[0,0,1]
	v_lshlrev_b32_e32 v8, 16, v10
	v_mul_f32_e32 v139, 0x3e0293ee, v8
	v_and_b32_e32 v8, 0xffff0000, v10
	v_mul_f32_e32 v8, 0x3e0293ee, v8
	v_cvt_pk_fp8_f32 v139, v139, v8
	v_lshlrev_b32_e32 v9, 16, v11
	v_mul_f32_e32 v8, 0x3e0293ee, v9
	v_and_b32_e32 v9, 0xffff0000, v11
	v_mul_f32_e32 v9, 0x3e0293ee, v9
	v_cvt_pk_fp8_f32 v139, v8, v9 op_sel:[0,0,1]
	v_lshlrev_b32_e32 v8, 16, v4
	v_and_b32_e32 v4, 0xffff0000, v4
	v_mul_f32_e32 v140, 0x3e0293ee, v8
	v_mul_f32_e32 v4, 0x3e0293ee, v4
	v_cvt_pk_fp8_f32 v140, v140, v4
	v_lshlrev_b32_e32 v8, 16, v5
	v_and_b32_e32 v5, 0xffff0000, v5
	v_mul_f32_e32 v4, 0x3e0293ee, v8
	v_mul_f32_e32 v5, 0x3e0293ee, v5
	v_cvt_pk_fp8_f32 v140, v4, v5 op_sel:[0,0,1]
	v_lshlrev_b32_e32 v4, 16, v6
	v_mul_f32_e32 v141, 0x3e0293ee, v4
	v_and_b32_e32 v4, 0xffff0000, v6
	v_mul_f32_e32 v4, 0x3e0293ee, v4
	v_cvt_pk_fp8_f32 v141, v141, v4
	v_lshlrev_b32_e32 v5, 16, v7
	v_mul_f32_e32 v4, 0x3e0293ee, v5
	v_and_b32_e32 v5, 0xffff0000, v7
	v_mul_f32_e32 v5, 0x3e0293ee, v5
	v_cvt_pk_fp8_f32 v141, v4, v5 op_sel:[0,0,1]
	v_lshlrev_b32_e32 v4, 16, v0
	v_and_b32_e32 v0, 0xffff0000, v0
	v_mul_f32_e32 v142, 0x3e0293ee, v4
	v_mul_f32_e32 v0, 0x3e0293ee, v0
	v_cvt_pk_fp8_f32 v142, v142, v0
	v_lshlrev_b32_e32 v4, 16, v1
; #define LAS __attribute__((address_space(3)))
; __device__ __forceinline__ float bflo(unsigned w) { return __uint_as_float(w << 16); }
; __device__ __forceinline__ float bfhi(unsigned w) { return __uint_as_float(w & 0xffff0000u); }
; #define SBAR() __builtin_amdgcn_sched_barrier(0)
; template <class P>
; __device__ __forceinline__ void sparse8_wave(P& pol, LAS unsigned char* wll, int lane) {
;     ...
;     f32x16 o[4] = {}; float m_reg = 0.f, l_reg = 0.f; f32x16 mneg = {}; f32x16 lacc = {}; bool seen = false;
;     const i32x8 ones8 = (i32x8){0x38383838, 0x38383838, 0x38383838, 0x38383838, 0x38383838, 0x38383838, 0x38383838, 0x38383838};
;     const int a0k = 32 * ((lane >> 5) & 1) + ((lane >> 3) & 3), che = (((lane & 7) ^ (lane >> 4)) & 7) << 4, cho = che ^ 64;
;     const int vcol0 = lane >> 2; const unsigned voff = (unsigned)vcol0 * SEQ + ((((lane & 3) ^ (vcol0 >> 2)) & 3) << 4);
;     const int nt = pol.ntiles();
;     typename P::TI ti, tn;
;     ...
;     pol.tile(0, ti);
;     SP8_DMA_K(ti); SP8_DMA_V(ti);
;     pol.pre_issue(); SBAR();
;     i32x8 qf[2];
;     { const bf16_t* Qw = pol.qptr(r32); u32x4 qv[2][4];
; #pragma unroll
;       for (int sK = 0; sK < 2; ++sK)
; #pragma unroll
;           for (int c = 0; c < 4; ++c) qv[sK][c] = *(const u32x4*)(Qw + 64 * sK + 32 * hi + 8 * c);
;       SBAR();
; #pragma unroll
;       for (int sK = 0; sK < 2; ++sK) { unsigned w[8];
; #pragma unroll
;           for (int c = 0; c < 4; ++c) { const u32x4 v = qv[sK][c];
;               w[2 * c] = pk4_fp8(bflo(v.x) * QCS, bfhi(v.x) * QCS, bflo(v.y) * QCS, bfhi(v.y) * QCS); w[2 * c + 1] = pk4_fp8(bflo(v.z) * QCS, bfhi(v.z) * QCS, bflo(v.w) * QCS, bfhi(v.w) * QCS); }
;           qf[sK] = (i32x8){(int)w[0], (int)w[1], (int)w[2], (int)w[3], (int)w[4], (int)w[5], (int)w[6], (int)w[7]}; } }
; __global__ void __launch_bounds__(NTHR, 2) fwd(Params p) {
;     ...
;                 for (int it = vcu; it < 1024; it += G) {
;                     const int tid2 = fresh_tid(wv), wid = __builtin_amdgcn_readfirstlane(tid2 >> 6), lane = tid2 & 63;
;                     const int w = it * 8 + wid; LAS unsigned char* wl = lds + wid * da::SP_WAVE_LDS;
;                     if constexpr (F8_SPARSE) { const unsigned char* ra8 = (const unsigned char*)RA; PolB8 pol; pol.init(Hx, Oat, ra8, ra8 + 32 * MiB, ra8 + 64 * MiB, ra8 + 96 * MiB, w, lane); d8::sparse8_wave(pol, wl, lane); }
	v_and_b32_e32 v1, 0xffff0000, v1
	v_mul_f32_e32 v0, 0x3e0293ee, v4
	v_mul_f32_e32 v1, 0x3e0293ee, v1
	v_cvt_pk_fp8_f32 v142, v0, v1 op_sel:[0,0,1]
	v_lshlrev_b32_e32 v0, 16, v2
	v_mul_f32_e32 v143, 0x3e0293ee, v0
	v_and_b32_e32 v0, 0xffff0000, v2
	v_mul_f32_e32 v0, 0x3e0293ee, v0
	s_add_i32 s38, s38, 1
	v_cvt_pk_fp8_f32 v143, v143, v0
	v_cvt_f32_ubyte0_e32 v0, s38
	v_exp_f32_e64 v0, -v0
	v_lshlrev_b32_e32 v1, 16, v3
	v_and_b32_e32 v2, 0xffff0000, v3
	v_mul_f32_e32 v1, 0x3e0293ee, v1
	v_mul_f32_e32 v2, 0x3e0293ee, v2
	v_or_b32_e32 v170, s57, v33
	v_cvt_pk_fp8_f32 v143, v1, v2 op_sel:[0,0,1]
	v_cvt_f32_ubyte0_e32 v1, s29
	v_mul_f32_e32 v169, 0xbfb8aa3b, v0
	v_subrev_u32_e32 v0, s25, v170
	v_cvt_f32_i32_e32 v2, v0
	v_rcp_iflag_f32_e32 v3, v1
	v_ashrrev_i32_e32 v0, 30, v0
	s_add_u32 s89, s1, s36
	v_add_u32_e32 v4, s24, v165
	v_mul_f32_e32 v3, v2, v3
	v_trunc_f32_e32 v3, v3
	v_fma_f32 v2, -v3, v1, v2
	v_cvt_i32_f32_e32 v3, v3
	v_or_b32_e32 v0, 1, v0
	v_cmp_ge_f32_e64 vcc, |v2|, v1
	s_addc_u32 s24, s33, 0
	s_add_i32 s0, s8, s55
	s_lshr_b32 s7, s56, 8
	s_lshl_b32 s7, s7, 5
	s_xor_b32 s0, s0, s7
	s_add_i32 s7, s54, s8
	v_cndmask_b32_e32 v0, 0, v0, vcc
	s_lshr_b32 s1, s0, 4
	s_bfe_u32 s0, s0, 0x30004
	s_and_b32 s7, s7, 15
	v_add_u32_e32 v0, v3, v0
	s_lshl_b32 s33, s7, 8
	s_lshl_b32 s7, s0, 3
	s_lshl_b32 s0, s0, 1
	v_sub_u32_sdwa v0, v4, sext(v0) dst_sel:DWORD dst_unused:UNUSED_PAD src0_sel:DWORD src1_sel:WORD_0
	s_sub_i32 s28, s28, s9
	s_and_b32 s29, s8, 3
	s_bfe_u32 s1, s1, 0x20001
	s_min_u32 s8, s7, 55
	s_min_u32 s9, s0, 13
	v_mul_f32_e32 v162, v169, v1
	v_cvt_f32_i32_e32 v164, v0
	v_lshlrev_b32_e32 v0, 1, v161
	v_lshrrev_b32_e32 v1, 1, v32
	s_max_u32 s6, s1, 1
	s_add_i32 s8, s8, s9
	s_min_u32 s1, s1, 2
	v_bfe_u32 v2, v32, 1, 3
	v_mov_b32_e32 v3, 0x1000
	v_lshrrev_b32_e32 v6, 2, v32
	v_bfe_u32 v7, v32, 2, 2
	v_bitop3_b32 v1, v0, v1, 7 bitop3:0x78
	s_add_i32 s8, s8, s1
	v_lshl_or_b32 v3, v163, 7, v3
	v_bitop3_b32 v6, v0, v6, 3 bitop3:0x78
	v_bitop3_b32 v7, v0, v7, 1 bitop3:0x36
	v_lshlrev_b32_e32 v173, 4, v1
	v_bitop3_b32 v1, v0, v2, 1 bitop3:0x36
	s_lshl_b32 s91, s6, 6
	s_sub_i32 s1, s8, s6
	s_max_u32 s6, s7, 1
	v_lshl_add_u32 v171, v160, 7, s61
	v_add_u32_e32 v172, s61, v3
	v_mul_i32_i24_e32 v3, 0xffffff84, v160
	v_lshlrev_b32_e32 v4, 4, v161
	v_lshl_add_u32 v5, v160, 6, s61
	v_lshlrev_b32_e32 v6, 4, v6
	v_lshlrev_b32_e32 v7, 4, v7
	v_lshlrev_b32_e32 v174, 4, v1
	v_bitop3_b32 v1, v0, v2, 4 bitop3:0x36
	v_bitop3_b32 v0, v0, v2, 5 bitop3:0x36
	s_sub_i32 s1, s1, s6
	s_max_u32 s0, s0, 1
	v_mov_b32_e32 v48, v233
	v_mov_b32_e32 v49, v233
	v_mov_b32_e32 v62, v233
	v_mov_b32_e32 v63, v233
	s_mov_b64 s[18:19], s[30:31]
	v_lshlrev_b32_e32 v175, 4, v1
	v_lshlrev_b32_e32 v176, 4, v0
	s_sub_i32 s25, s23, s60
	s_sub_i32 s23, s1, s0
	v_mov_b32_e32 v50, v233
	v_mov_b32_e32 v51, v233
	v_mov_b32_e32 v52, v233
	v_mov_b32_e32 v53, v233
	v_mov_b32_e32 v54, v233
	v_mov_b32_e32 v55, v233
	v_mov_b32_e32 v56, v233
	v_mov_b32_e32 v57, v233
	v_mov_b32_e32 v58, v233
	v_mov_b32_e32 v59, v233
	v_mov_b32_e32 v60, v233
	v_mov_b32_e32 v61, v233
	v_mov_b32_e32 v177, 0
	v_add_u32_e32 v178, v171, v3
	v_add_u32_e32 v179, s61, v4
	v_add_u32_e32 v180, v5, v6
	v_add_u32_e32 v181, v5, v7
	v_mov_b64_e32 v[78:79], v[62:63]
	v_mov_b64_e32 v[32:33], v[48:49]
	v_mov_b64_e32 v[0:1], v[48:49]
	v_mov_b64_e32 v[16:17], v[48:49]
	s_mov_b32 s30, 0x41800000
	s_mov_b32 s88, 0
	v_cmp_gt_u32_e64 s[38:39], 32, v163
	s_add_i32 s28, s28, 0x3fffffc
	s_lshl_b32 s90, s29, 10
	s_add_i32 s23, s23, 17
	s_mov_b64 s[0:1], 0
	v_mov_b64_e32 v[76:77], v[60:61]
	v_mov_b64_e32 v[74:75], v[58:59]
	v_mov_b64_e32 v[72:73], v[56:57]
	v_mov_b64_e32 v[70:71], v[54:55]
	v_mov_b64_e32 v[68:69], v[52:53]
	v_mov_b64_e32 v[66:67], v[50:51]
	v_mov_b64_e32 v[64:65], v[48:49]
	v_mov_b64_e32 v[34:35], v[50:51]
	v_mov_b64_e32 v[36:37], v[52:53]
	v_mov_b64_e32 v[38:39], v[54:55]
	v_mov_b64_e32 v[40:41], v[56:57]
	v_mov_b64_e32 v[42:43], v[58:59]
	v_mov_b64_e32 v[44:45], v[60:61]
	v_mov_b64_e32 v[46:47], v[62:63]
	v_mov_b64_e32 v[2:3], v[50:51]
	v_mov_b64_e32 v[4:5], v[52:53]
	v_mov_b64_e32 v[6:7], v[54:55]
	v_mov_b64_e32 v[8:9], v[56:57]
	v_mov_b64_e32 v[10:11], v[58:59]
	v_mov_b64_e32 v[12:13], v[60:61]
	v_mov_b64_e32 v[14:15], v[62:63]
	v_mov_b64_e32 v[18:19], v[50:51]
	v_mov_b64_e32 v[20:21], v[52:53]
	v_mov_b64_e32 v[22:23], v[54:55]
	v_mov_b64_e32 v[24:25], v[56:57]
	v_mov_b64_e32 v[26:27], v[58:59]
	v_mov_b64_e32 v[28:29], v[60:61]
	v_mov_b64_e32 v[30:31], v[62:63]
	v_mov_b32_e32 v80, 0
	v_mov_b32_e32 v81, v177
	v_mov_b32_e32 v82, v177
	v_mov_b32_e32 v83, v177
	v_mov_b32_e32 v84, v177
	v_mov_b32_e32 v85, v177
	v_mov_b32_e32 v86, v177
	v_mov_b32_e32 v87, v177
	v_mov_b32_e32 v88, v177
	v_mov_b32_e32 v89, v177
	v_mov_b32_e32 v90, v177
	v_mov_b32_e32 v91, v177
	v_mov_b32_e32 v92, v177
	v_mov_b32_e32 v93, v177
	v_mov_b32_e32 v94, v177
	v_mov_b32_e32 v95, v177
	s_mov_b32 s31, 0x41880000
	v_add_u32_e32 v216, v171, v173
	v_add_u32_e32 v217, v171, v174
	v_add_u32_e32 v218, v172, v173
	v_add_u32_e32 v219, v172, v174
	v_add_u32_e32 v220, v171, v175
	v_add_u32_e32 v221, v171, v176
	v_add_u32_e32 v222, v172, v175
	v_add_u32_e32 v223, v172, v176
	v_mov_b32_e32 v209, v208
	v_mov_b32_e32 v210, v208
	v_mov_b32_e32 v211, v208
	v_mov_b32_e32 v212, v208
	v_mov_b32_e32 v213, v208
	v_mov_b32_e32 v214, v208
	v_mov_b32_e32 v215, v208
